# FFN-front pre-norm loop prefetch rotation with a counted wait behind the group's 16 stores (stores stay in flight)
# speedup vs baseline: 1.0076x; 1.0076x over previous
; DEV int otid() { int t = threadIdx.x; asm volatile("" : "+v"(t)); return t; }
; DEV unsigned char* ows_(unsigned char* w) { gptr_t g = (gptr_t)w; asm volatile("" : "+s"(g)); return (unsigned char*)g; }
; template <int ROWS> DEV void ffn_front_unit(const Params& p, int layer, int m0, LAS char* lds) {
;     unsigned char* ws = ows_(p.ws); const int tid = otid(), lane = tid & 63, wid = tid >> 6;
;     const float* mod = (const float*)(ws + WS_MOD) + (size_t)layer * 3 * 6144;
;     const float* mu = mod + mod_row(m0) * 6144;
;     const NormRegs nr = norm_regs(p.norm_ffn + layer * 1024, mu + 3072, mu + 4096, lane);
;     for (int r0 = wid * 4; r0 < ROWS; r0 += 32) {
;         float xv[4][2][8];
; #pragma unroll
;         for (int q = 0; q < 4; ++q) load_row_bf((const bf16_t*)(ws + WS_X) + (size_t)(m0 + r0 + q) * 1024, xv[q], lane);
; #pragma unroll
;         for (int q = 0; q < 4; ++q) norm_store_ffn(p, m0 + r0 + q, xv[q], nr, lane); }
.LBB0_1087:
	s_mov_b64 s[8:9], s[56:57]
	v_mov_b32_e32 v111, v246
	s_movk_i32 s2, 0x80
	v_ashrrev_i32_e32 v2, 4, v111
	v_and_b32_e32 v36, -4, v2
	v_cmp_gt_i32_e32 vcc, s2, v36
	s_and_saveexec_b64 s[40:41], vcc
	s_cbranch_execz .LBB0_1090
	s_mul_i32 s2, s72, 0x12000
	s_add_u32 s2, s8, s2
	s_addc_u32 s3, s9, 0
	s_lshr_b32 s19, s18, 7
	s_mul_i32 s20, s19, 0x1800
	s_ashr_i32 s21, s20, 31
	s_lshl_b64 s[20:21], s[20:21], 2
	s_add_u32 s2, s2, s20
	s_addc_u32 s3, s3, s21
	v_lshlrev_b32_e32 v2, 3, v111
	s_add_u32 s20, s2, 0x13000
	v_and_b32_e32 v34, 0x1f8, v2
	s_addc_u32 s21, s3, 0
	v_lshlrev_b32_e32 v30, 2, v34
	s_add_u32 s28, s2, 0x14000
	v_or_b32_e32 v10, 0x800, v30
	s_addc_u32 s29, s3, 0
	global_load_dwordx4 v[2:5], v10, s[20:21]
	global_load_dwordx4 v[6:9], v10, s[20:21] offset:16
	global_load_dwordx4 v[38:41], v10, s[28:29] offset:16
	global_load_dwordx4 v[42:45], v10, s[28:29]
	s_nop 0
	global_load_dwordx4 v[10:13], v30, s[4:5] offset:2048
	global_load_dwordx4 v[14:17], v30, s[4:5] offset:2064
	global_load_dwordx4 v[18:21], v30, s[20:21]
	global_load_dwordx4 v[22:25], v30, s[20:21] offset:16
	global_load_dwordx4 v[46:49], v30, s[28:29] offset:16
	global_load_dwordx4 v[50:53], v30, s[28:29]
	global_load_dwordx4 v[26:29], v30, s[4:5]
	s_nop 0
	global_load_dwordx4 v[30:33], v30, s[4:5] offset:16
	v_mov_b32_e32 v35, v179
	v_subrev_u32_e32 v112, 32, v36
	v_and_b32_e32 v37, 63, v111
	v_lshlrev_b32_e32 v178, 4, v37
	s_mov_b64 s[42:43], 0
	s_mov_b64 s[44:45], s[56:57]
	s_waitcnt vmcnt(0)
	v_pk_add_f32 v[68:69], v[38:39], 1.0 op_sel_hi:[1,0]
	v_add_u32_e32 v38, s17, v36
	v_pk_add_f32 v[72:73], v[40:41], 1.0 op_sel_hi:[1,0]
	v_ashrrev_i32_e32 v39, 31, v38
	v_mov_b64_e32 v[40:41], s[56:57]
	v_mad_i64_i32 v[74:75], s[20:21], v38, s95, v[40:41]
	v_mad_i64_i32 v[76:77], s[20:21], v38, s95, v[34:35]
	v_lshlrev_b64 v[38:39], 11, v[38:39]
	v_lshl_add_u64 v[78:79], s[8:9], 0, v[38:39]
	v_add_u32_e32 v38, s16, v36
	v_ashrrev_i32_e32 v39, 31, v38
	v_mad_i64_i32 v[80:81], s[20:21], v38, s95, v[40:41]
	v_mad_i64_i32 v[82:83], s[20:21], v38, s95, v[34:35]
	v_lshlrev_b64 v[38:39], 11, v[38:39]
	v_lshl_add_u64 v[84:85], s[8:9], 0, v[38:39]
	v_add_u32_e32 v38, s13, v36
	v_add_u32_e32 v36, s12, v36
	v_ashrrev_i32_e32 v39, 31, v38
	v_ashrrev_i32_e32 v37, 31, v36
	v_mad_i64_i32 v[86:87], s[20:21], v38, s95, v[40:41]
	v_mad_i64_i32 v[88:89], s[20:21], v38, s95, v[34:35]
	v_lshlrev_b64 v[38:39], 11, v[38:39]
	v_mad_i64_i32 v[94:95], s[20:21], v36, s95, v[34:35]
	v_lshlrev_b64 v[34:35], 11, v[36:37]
	v_pk_add_f32 v[58:59], v[50:51], 1.0 op_sel_hi:[1,0]
	v_pk_add_f32 v[60:61], v[46:47], 1.0 op_sel_hi:[1,0]
	v_pk_add_f32 v[62:63], v[52:53], 1.0 op_sel_hi:[1,0]
	v_pk_add_f32 v[64:65], v[48:49], 1.0 op_sel_hi:[1,0]
	v_pk_add_f32 v[66:67], v[42:43], 1.0 op_sel_hi:[1,0]
	v_pk_add_f32 v[70:71], v[44:45], 1.0 op_sel_hi:[1,0]
	v_lshl_add_u64 v[90:91], s[8:9], 0, v[38:39]
	v_mad_i64_i32 v[92:93], s[20:21], v36, s95, v[40:41]
	v_lshl_add_u64 v[96:97], s[8:9], 0, v[34:35]
	v_lshl_add_u64 v[182:183], v[96:97], 0, v[178:179]
	v_add_co_u32_e32 v182, vcc, 0x19510000, v182
	s_nop 1
	v_addc_co_u32_e32 v183, vcc, 0, v183, vcc
	global_load_dwordx4 v[148:151], v[182:183], off offset:256
	global_load_dwordx4 v[152:155], v[182:183], off offset:1280
	v_lshl_add_u64 v[182:183], v[90:91], 0, v[178:179]
	v_add_co_u32_e32 v182, vcc, s34, v182
	s_nop 1
	v_addc_co_u32_e32 v183, vcc, 0, v183, vcc
	global_load_dwordx4 v[156:159], v[182:183], off offset:256
	global_load_dwordx4 v[166:169], v[182:183], off offset:1280
	v_lshl_add_u64 v[182:183], v[84:85], 0, v[178:179]
	v_add_co_u32_e32 v182, vcc, s34, v182
	s_nop 1
	v_addc_co_u32_e32 v183, vcc, 0, v183, vcc
	global_load_dwordx4 v[170:173], v[182:183], off offset:256
	global_load_dwordx4 v[174:177], v[182:183], off offset:1280
	v_lshl_add_u64 v[182:183], v[78:79], 0, v[178:179]
	v_add_co_u32_e32 v182, vcc, s34, v182
	s_nop 1
	v_addc_co_u32_e32 v183, vcc, 0, v183, vcc
	global_load_dwordx4 v[198:201], v[182:183], off offset:256
	global_load_dwordx4 v[202:205], v[182:183], off offset:1280
	v_lshl_add_u64 v[78:79], v[78:79], 0, s[14:15]
	v_lshl_add_u64 v[84:85], v[84:85], 0, s[14:15]
	v_lshl_add_u64 v[90:91], v[90:91], 0, s[14:15]
	v_lshl_add_u64 v[96:97], v[96:97], 0, s[14:15]
	s_waitcnt vmcnt(0)
; DEV float bflo(unsigned u) { return __uint_as_float(u << 16); }
; DEV float bfhi(unsigned u) { return __uint_as_float(u & 0xffff0000u); }
; DEV float fast_rsq(float x) { return __builtin_amdgcn_rsqf(x); }
; DEV float wave_sum(float v) { v = half_sum(v); v += lx16(v); v += lr8(v); v += lr4(v); v += lx2(v); v += lx1(v); return v; }
; DEV void norm_store_ffn(const Params& p, int tok, const float (&xv)[2][8], const NormRegs& nr, int lane) {
;     float ss = 0.f;
; #pragma unroll
;     for (int j = 0; j < 2; ++j)
; #pragma unroll
;         for (int i = 0; i < 8; ++i) ss += xv[j][i] * xv[j][i];
;     ss = wave_sum(ss);
;     const float rinv = fast_rsq(ss * (1.0f / 1024.0f) + EPS);
; DEV void load_row_bf(const bf16_t* __restrict__ src, float (&xv)[2][8], int lane) {
; #pragma unroll
;     for (int j = 0; j < 2; ++j) { const u32x4 a = *(const u32x4*)(src + 8 * lane + 512 * j);
; #pragma unroll
;         for (int e = 0; e < 4; ++e) { xv[j][2 * e] = bflo(a[e]); xv[j][2 * e + 1] = bfhi(a[e]); } }
; }
.LBB0_1089:
	v_mov_b64_e32 v[98:99], v[148:149]
	v_mov_b64_e32 v[100:101], v[150:151]
	v_mov_b64_e32 v[114:115], v[152:153]
	v_mov_b64_e32 v[116:117], v[154:155]
	v_mov_b64_e32 v[54:55], v[156:157]
	v_mov_b64_e32 v[56:57], v[158:159]
	v_mov_b64_e32 v[50:51], v[166:167]
	v_mov_b64_e32 v[52:53], v[168:169]
	v_mov_b64_e32 v[46:47], v[170:171]
	v_mov_b64_e32 v[48:49], v[172:173]
	v_mov_b64_e32 v[42:43], v[174:175]
	v_mov_b64_e32 v[44:45], v[176:177]
	v_mov_b64_e32 v[38:39], v[198:199]
	v_mov_b64_e32 v[40:41], v[200:201]
	v_mov_b64_e32 v[34:35], v[202:203]
	v_mov_b64_e32 v[36:37], v[204:205]
	v_lshl_add_u64 v[106:107], s[44:45], 0, v[94:95]
	v_lshl_add_u64 v[104:105], v[92:93], 0, v[178:179]
	v_add_u32_e32 v112, 32, v112
	s_movk_i32 s2, 0x5f
	v_add_co_u32_e32 v106, vcc, s35, v106
	s_nop 1
	v_addc_co_u32_e32 v107, vcc, 0, v107, vcc
	v_add_co_u32_e32 v104, vcc, s35, v104
	s_nop 1
	v_addc_co_u32_e32 v105, vcc, 0, v105, vcc
	v_lshl_add_u64 v[92:93], v[92:93], 0, s[24:25]
	v_lshl_add_u64 v[182:183], v[96:97], 0, v[178:179]
	v_add_co_u32_e32 v182, vcc, 0x19510000, v182
	s_nop 1
	v_addc_co_u32_e32 v183, vcc, 0, v183, vcc
	global_load_dwordx4 v[148:151], v[182:183], off offset:256
	global_load_dwordx4 v[152:155], v[182:183], off offset:1280
	v_lshl_add_u64 v[182:183], v[90:91], 0, v[178:179]
	v_add_co_u32_e32 v182, vcc, s34, v182
	s_nop 1
	v_addc_co_u32_e32 v183, vcc, 0, v183, vcc
	global_load_dwordx4 v[156:159], v[182:183], off offset:256
	global_load_dwordx4 v[166:169], v[182:183], off offset:1280
	v_lshl_add_u64 v[182:183], v[84:85], 0, v[178:179]
	v_add_co_u32_e32 v182, vcc, s34, v182
	s_nop 1
	v_addc_co_u32_e32 v183, vcc, 0, v183, vcc
	global_load_dwordx4 v[170:173], v[182:183], off offset:256
	global_load_dwordx4 v[174:177], v[182:183], off offset:1280
	v_lshl_add_u64 v[182:183], v[78:79], 0, v[178:179]
	v_add_co_u32_e32 v182, vcc, s34, v182
	s_nop 1
	v_addc_co_u32_e32 v183, vcc, 0, v183, vcc
	global_load_dwordx4 v[198:201], v[182:183], off offset:256
	global_load_dwordx4 v[202:205], v[182:183], off offset:1280
	v_lshl_add_u64 v[78:79], v[78:79], 0, s[14:15]
	v_lshl_add_u64 v[84:85], v[84:85], 0, s[14:15]
	v_lshl_add_u64 v[90:91], v[90:91], 0, s[14:15]
	v_lshl_add_u64 v[96:97], v[96:97], 0, s[14:15]
	v_lshlrev_b32_e32 v130, 16, v98
	v_and_b32_e32 v131, 0xffff0000, v98
	v_lshlrev_b32_e32 v126, 16, v99
	v_and_b32_e32 v127, 0xffff0000, v99
	v_pk_mul_f32 v[132:133], v[130:131], v[130:131]
	v_pk_mul_f32 v[128:129], v[126:127], v[126:127]
	v_add_f32_e32 v110, v132, v133
	v_lshlrev_b32_e32 v122, 16, v100
	v_and_b32_e32 v123, 0xffff0000, v100
	v_add_f32_e32 v110, v128, v110
	v_pk_mul_f32 v[124:125], v[122:123], v[122:123]
	v_add_f32_e32 v110, v129, v110
	v_lshlrev_b32_e32 v118, 16, v101
	v_and_b32_e32 v119, 0xffff0000, v101
	v_add_f32_e32 v110, v124, v110
	v_pk_mul_f32 v[120:121], v[118:119], v[118:119]
	v_add_f32_e32 v110, v125, v110
	v_lshlrev_b32_e32 v108, 16, v114
	v_and_b32_e32 v109, 0xffff0000, v114
	v_add_f32_e32 v110, v120, v110
	v_lshlrev_b32_e32 v100, 16, v115
	v_and_b32_e32 v101, 0xffff0000, v115
	v_pk_mul_f32 v[114:115], v[108:109], v[108:109]
	v_add_f32_e32 v110, v121, v110
	v_add_f32_e32 v110, v114, v110
	v_pk_mul_f32 v[136:137], v[100:101], v[100:101]
	v_add_f32_e32 v110, v115, v110
	v_lshlrev_b32_e32 v102, 16, v116
	v_and_b32_e32 v103, 0xffff0000, v116
	v_add_f32_e32 v110, v136, v110
	v_lshlrev_b32_e32 v98, 16, v117
	v_and_b32_e32 v99, 0xffff0000, v117
	v_pk_mul_f32 v[116:117], v[102:103], v[102:103]
	v_add_f32_e32 v110, v137, v110
	v_add_f32_e32 v110, v116, v110
	v_pk_mul_f32 v[134:135], v[98:99], v[98:99]
	v_add_f32_e32 v110, v117, v110
	v_add_f32_e32 v110, v134, v110
	v_add_f32_e32 v110, v135, v110
	v_mov_b32_e32 v113, v110
	s_nop 1
	v_permlane32_swap_b32 v110, v113
	s_nop 1
	s_nop 0
	v_add_f32_e32 v110, v110, v113
	ds_swizzle_b32 v113, v110 offset:swizzle(SWAP,16)
	s_waitcnt lgkmcnt(0)
	v_add_f32_e32 v110, v110, v113
	s_nop 1
	v_add_f32_dpp v110, v110, v110 row_ror:8 row_mask:0xf bank_mask:0xf bound_ctrl:1
	s_nop 1
	v_add_f32_dpp v110, v110, v110 row_ror:4 row_mask:0xf bank_mask:0xf bound_ctrl:1
	s_nop 1
	v_add_f32_dpp v110, v110, v110 quad_perm:[2,3,0,1] row_mask:0xf bank_mask:0xf bound_ctrl:1
	s_nop 1
	v_add_f32_dpp v110, v110, v110 quad_perm:[1,0,3,2] row_mask:0xf bank_mask:0xf bound_ctrl:1
	v_fmamk_f32 v110, v110, 0x3a800000, v0
	v_rsq_f32_e32 v110, v110
	s_nop 0
	v_pk_mul_f32 v[114:115], v[110:111], v[130:131] op_sel_hi:[0,1]
	v_pk_mul_f32 v[116:117], v[110:111], v[122:123] op_sel_hi:[0,1]
	v_pk_mul_f32 v[114:115], v[26:27], v[114:115]
	v_pk_mul_f32 v[116:117], v[30:31], v[116:117]
	v_pk_fma_f32 v[114:115], v[58:59], v[114:115], v[18:19]
	v_pk_fma_f32 v[116:117], v[60:61], v[116:117], v[22:23]
	v_mov_b32_e32 v122, 0
	v_mov_b32_e32 v123, 0
	v_cvt_pk_fp8_f32 v122, v114, v115
	v_cvt_pk_fp8_f32 v123, v116, v117
	v_pk_mul_f32 v[120:121], v[110:111], v[126:127] op_sel_hi:[0,1]
	v_pk_mul_f32 v[118:119], v[110:111], v[118:119] op_sel_hi:[0,1]
	v_pk_mul_f32 v[120:121], v[28:29], v[120:121]
	v_pk_mul_f32 v[118:119], v[32:33], v[118:119]
	v_pk_fma_f32 v[120:121], v[62:63], v[120:121], v[20:21]
	v_pk_fma_f32 v[118:119], v[64:65], v[118:119], v[24:25]
	v_cvt_pk_fp8_f32 v122, v120, v121 op_sel:[0,0,1]
	v_cvt_pk_fp8_f32 v123, v118, v119 op_sel:[0,0,1]
	v_pk_mul_f32 v[108:109], v[110:111], v[108:109] op_sel_hi:[0,1]
	v_pk_mul_f32 v[102:103], v[110:111], v[102:103] op_sel_hi:[0,1]
	v_pk_mul_f32 v[98:99], v[110:111], v[98:99] op_sel_hi:[0,1]
	v_cvt_pk_f16_f32 v114, v114, v115
	v_cvt_pk_f16_f32 v115, v120, v121
	v_cvt_pk_f16_f32 v116, v116, v117
	v_cvt_pk_f16_f32 v117, v118, v119
	v_pk_mul_f32 v[108:109], v[10:11], v[108:109]
; DEV unsigned cvtpk_h(float lo, float hi) { f32x2 v = {lo, hi}; f16x2 r = __builtin_convertvector(v, f16x2); return __builtin_bit_cast(unsigned, r); }
; DEV unsigned pk_fp8x4(float a, float b, float c, float d) { int w = __builtin_amdgcn_cvt_pk_fp8_f32(a, b, 0, false); w = __builtin_amdgcn_cvt_pk_fp8_f32(c, d, w, true); return (unsigned)w; }
; DEV float fast_rsq(float x) { return __builtin_amdgcn_rsqf(x); }
; DEV float wave_sum(float v) { v = half_sum(v); v += lx16(v); v += lr8(v); v += lr4(v); v += lx2(v); v += lx1(v); return v; }
; DEV void norm_store_ffn(const Params& p, int tok, const float (&xv)[2][8], const NormRegs& nr, int lane) {
;     float ss = 0.f;
; #pragma unroll
;     for (int j = 0; j < 2; ++j)
; #pragma unroll
;         for (int i = 0; i < 8; ++i) ss += xv[j][i] * xv[j][i];
;     ss = wave_sum(ss);
;     const float rinv = fast_rsq(ss * (1.0f / 1024.0f) + EPS);
;     bf16_t* H = (bf16_t*)(p.ws + WS_H) + (size_t)tok * HLD;
; #pragma unroll
;     for (int j = 0; j < 2; ++j) { const int col = 8 * lane + 512 * j; float y[8];
; #pragma unroll
;         for (int i = 0; i < 4; ++i) { y[i] = xv[j][i] * rinv * nr.g[j][0][i] * (1.0f + nr.s[j][0][i]) + nr.h[j][0][i]; y[4 + i] = xv[j][4 + i] * rinv * nr.g[j][1][i] * (1.0f + nr.s[j][1][i]) + nr.h[j][1][i]; }
;         *(u32x2*)((unsigned char*)H + col) = (u32x2){pk_fp8x4(y[0], y[1], y[2], y[3]), pk_fp8x4(y[4], y[5], y[6], y[7])};
;         const u32x4 wl = {cvtpk_h(y[0], y[1]), cvtpk_h(y[2], y[3]), cvtpk_h(y[4], y[5]), cvtpk_h(y[6], y[7])};
;         *(u32x4*)(H + 1024 + col) = wl; }
	v_pk_mul_f32 v[102:103], v[14:15], v[102:103]
	v_pk_mul_f32 v[98:99], v[16:17], v[98:99]
	global_store_dwordx2 v[106:107], v[122:123], off offset:256
	global_store_dwordx4 v[104:105], v[114:117], off offset:2304
	v_pk_fma_f32 v[108:109], v[66:67], v[108:109], v[2:3]
	v_pk_fma_f32 v[102:103], v[68:69], v[102:103], v[6:7]
	v_pk_fma_f32 v[114:115], v[72:73], v[98:99], v[8:9]
	v_mov_b32_e32 v98, 0
	v_mov_b32_e32 v99, 0
	v_cvt_pk_fp8_f32 v98, v108, v109
	v_cvt_pk_fp8_f32 v99, v102, v103
	v_pk_mul_f32 v[100:101], v[110:111], v[100:101] op_sel_hi:[0,1]
	v_pk_mul_f32 v[100:101], v[12:13], v[100:101]
	v_lshlrev_b32_e32 v120, 16, v54
	v_pk_fma_f32 v[100:101], v[70:71], v[100:101], v[4:5]
	v_cvt_pk_fp8_f32 v99, v114, v115 op_sel:[0,0,1]
	v_cvt_pk_fp8_f32 v98, v100, v101 op_sel:[0,0,1]
	v_and_b32_e32 v121, 0xffff0000, v54
	v_lshlrev_b32_e32 v116, 16, v55
	v_and_b32_e32 v117, 0xffff0000, v55
	v_pk_mul_f32 v[122:123], v[120:121], v[120:121]
	v_pk_mul_f32 v[118:119], v[116:117], v[116:117]
	v_add_f32_e32 v110, v122, v123
	global_store_dwordx2 v[106:107], v[98:99], off offset:768
	v_cvt_pk_f16_f32 v98, v108, v109
	v_lshlrev_b32_e32 v108, 16, v56
	v_and_b32_e32 v109, 0xffff0000, v56
	v_add_f32_e32 v110, v118, v110
	v_cvt_pk_f16_f32 v99, v100, v101
	v_cvt_pk_f16_f32 v100, v102, v103
	v_cvt_pk_f16_f32 v101, v114, v115
	v_pk_mul_f32 v[114:115], v[108:109], v[108:109]
	v_add_f32_e32 v110, v119, v110
	global_store_dwordx4 v[104:105], v[98:101], off offset:3328
	v_lshlrev_b32_e32 v104, 16, v57
	v_and_b32_e32 v105, 0xffff0000, v57
	v_add_f32_e32 v110, v114, v110
	v_pk_mul_f32 v[106:107], v[104:105], v[104:105]
	v_add_f32_e32 v110, v115, v110
	v_lshlrev_b32_e32 v102, 16, v50
	v_and_b32_e32 v103, 0xffff0000, v50
	v_add_f32_e32 v106, v106, v110
	v_lshlrev_b32_e32 v54, 16, v53
	v_and_b32_e32 v55, 0xffff0000, v53
	v_lshlrev_b32_e32 v56, 16, v52
	v_and_b32_e32 v57, 0xffff0000, v52
	v_lshlrev_b32_e32 v52, 16, v51
	v_and_b32_e32 v53, 0xffff0000, v51
	v_pk_mul_f32 v[50:51], v[102:103], v[102:103]
	v_add_f32_e32 v106, v107, v106
	v_add_f32_e32 v50, v50, v106
	v_pk_mul_f32 v[128:129], v[52:53], v[52:53]
	v_add_f32_e32 v50, v51, v50
	v_add_f32_e32 v50, v128, v50
	v_pk_mul_f32 v[126:127], v[56:57], v[56:57]
	v_add_f32_e32 v50, v129, v50
	v_add_f32_e32 v50, v126, v50
	v_pk_mul_f32 v[124:125], v[54:55], v[54:55]
	v_add_f32_e32 v50, v127, v50
	v_add_f32_e32 v50, v124, v50
	v_add_f32_e32 v50, v125, v50
	v_mov_b32_e32 v51, v50
	s_nop 1
	v_permlane32_swap_b32 v50, v51
	s_nop 1
	v_lshl_add_u64 v[100:101], s[44:45], 0, v[88:89]
	v_add_f32_e32 v50, v50, v51
	ds_swizzle_b32 v51, v50 offset:swizzle(SWAP,16)
	v_add_co_u32_e32 v100, vcc, s35, v100
	v_lshl_add_u64 v[98:99], v[86:87], 0, v[178:179]
	s_nop 0
	v_addc_co_u32_e32 v101, vcc, 0, v101, vcc
	s_waitcnt lgkmcnt(0)
	v_add_f32_e32 v50, v50, v51
	v_add_co_u32_e32 v98, vcc, s35, v98
	s_nop 0
	v_add_f32_dpp v50, v50, v50 row_ror:8 row_mask:0xf bank_mask:0xf bound_ctrl:1
	v_addc_co_u32_e32 v99, vcc, 0, v99, vcc
	s_nop 0
	v_add_f32_dpp v50, v50, v50 row_ror:4 row_mask:0xf bank_mask:0xf bound_ctrl:1
	v_lshl_add_u64 v[86:87], v[86:87], 0, s[24:25]
	s_nop 0
	v_add_f32_dpp v50, v50, v50 quad_perm:[2,3,0,1] row_mask:0xf bank_mask:0xf bound_ctrl:1
	s_nop 1
	v_add_f32_dpp v50, v50, v50 quad_perm:[1,0,3,2] row_mask:0xf bank_mask:0xf bound_ctrl:1
	v_fmamk_f32 v50, v50, 0x3a800000, v0
	v_rsq_f32_e32 v50, v50
	s_nop 0
	v_pk_mul_f32 v[106:107], v[50:51], v[120:121] op_sel_hi:[0,1]
	v_pk_mul_f32 v[108:109], v[50:51], v[108:109] op_sel_hi:[0,1]
	v_pk_mul_f32 v[104:105], v[50:51], v[104:105] op_sel_hi:[0,1]
	v_pk_mul_f32 v[106:107], v[26:27], v[106:107]
	v_pk_mul_f32 v[108:109], v[30:31], v[108:109]
	v_pk_mul_f32 v[104:105], v[32:33], v[104:105]
	v_pk_fma_f32 v[106:107], v[58:59], v[106:107], v[18:19]
	v_pk_fma_f32 v[108:109], v[60:61], v[108:109], v[22:23]
	v_pk_mul_f32 v[114:115], v[50:51], v[116:117] op_sel_hi:[0,1]
	v_pk_fma_f32 v[116:117], v[64:65], v[104:105], v[24:25]
	v_mov_b32_e32 v104, 0
	v_mov_b32_e32 v105, 0
	v_cvt_pk_fp8_f32 v104, v106, v107
	v_cvt_pk_fp8_f32 v105, v108, v109
	v_pk_mul_f32 v[102:103], v[50:51], v[102:103] op_sel_hi:[0,1]
	v_pk_mul_f32 v[56:57], v[50:51], v[56:57] op_sel_hi:[0,1]
	v_pk_mul_f32 v[52:53], v[50:51], v[52:53] op_sel_hi:[0,1]
	v_pk_mul_f32 v[50:51], v[50:51], v[54:55] op_sel_hi:[0,1]
	v_pk_mul_f32 v[102:103], v[10:11], v[102:103]
	v_pk_mul_f32 v[56:57], v[14:15], v[56:57]
	v_pk_mul_f32 v[50:51], v[16:17], v[50:51]
	v_pk_mul_f32 v[114:115], v[28:29], v[114:115]
	v_pk_fma_f32 v[102:103], v[66:67], v[102:103], v[2:3]
	v_pk_fma_f32 v[56:57], v[68:69], v[56:57], v[6:7]
	v_pk_fma_f32 v[54:55], v[72:73], v[50:51], v[8:9]
	v_mov_b32_e32 v50, 0
	v_mov_b32_e32 v51, 0
	v_pk_fma_f32 v[114:115], v[62:63], v[114:115], v[20:21]
	v_cvt_pk_fp8_f32 v50, v102, v103
	v_cvt_pk_fp8_f32 v51, v56, v57
	v_cvt_pk_fp8_f32 v104, v114, v115 op_sel:[0,0,1]
	v_cvt_pk_fp8_f32 v105, v116, v117 op_sel:[0,0,1]
	v_pk_mul_f32 v[52:53], v[12:13], v[52:53]
	v_cvt_pk_fp8_f32 v51, v54, v55 op_sel:[0,0,1]
	v_pk_fma_f32 v[52:53], v[70:71], v[52:53], v[4:5]
	global_store_dwordx2 v[100:101], v[104:105], off offset:256
	v_cvt_pk_fp8_f32 v50, v52, v53 op_sel:[0,0,1]
	v_cvt_pk_f16_f32 v104, v106, v107
	v_cvt_pk_f16_f32 v105, v114, v115
	v_cvt_pk_f16_f32 v106, v108, v109
	v_cvt_pk_f16_f32 v107, v116, v117
	v_lshlrev_b32_e32 v108, 16, v46
	v_and_b32_e32 v109, 0xffff0000, v46
	global_store_dwordx4 v[98:99], v[104:107], off offset:2304
	v_pk_mul_f32 v[114:115], v[108:109], v[108:109]
	global_store_dwordx2 v[100:101], v[50:51], off offset:768
	v_lshlrev_b32_e32 v104, 16, v47
	v_and_b32_e32 v105, 0xffff0000, v47
	v_pk_mul_f32 v[106:107], v[104:105], v[104:105]
; DEV unsigned cvtpk_h(float lo, float hi) { f32x2 v = {lo, hi}; f16x2 r = __builtin_convertvector(v, f16x2); return __builtin_bit_cast(unsigned, r); }
; DEV unsigned pk_fp8x4(float a, float b, float c, float d) { int w = __builtin_amdgcn_cvt_pk_fp8_f32(a, b, 0, false); w = __builtin_amdgcn_cvt_pk_fp8_f32(c, d, w, true); return (unsigned)w; }
; DEV float fast_rsq(float x) { return __builtin_amdgcn_rsqf(x); }
; DEV float wave_sum(float v) { v = half_sum(v); v += lx16(v); v += lr8(v); v += lr4(v); v += lx2(v); v += lx1(v); return v; }
; DEV void norm_store_ffn(const Params& p, int tok, const float (&xv)[2][8], const NormRegs& nr, int lane) {
;     float ss = 0.f;
; #pragma unroll
;     for (int j = 0; j < 2; ++j)
; #pragma unroll
;         for (int i = 0; i < 8; ++i) ss += xv[j][i] * xv[j][i];
;     ss = wave_sum(ss);
;     const float rinv = fast_rsq(ss * (1.0f / 1024.0f) + EPS);
;     bf16_t* H = (bf16_t*)(p.ws + WS_H) + (size_t)tok * HLD;
; #pragma unroll
;     for (int j = 0; j < 2; ++j) { const int col = 8 * lane + 512 * j; float y[8];
; #pragma unroll
;         for (int i = 0; i < 4; ++i) { y[i] = xv[j][i] * rinv * nr.g[j][0][i] * (1.0f + nr.s[j][0][i]) + nr.h[j][0][i]; y[4 + i] = xv[j][4 + i] * rinv * nr.g[j][1][i] * (1.0f + nr.s[j][1][i]) + nr.h[j][1][i]; }
;         *(u32x2*)((unsigned char*)H + col) = (u32x2){pk_fp8x4(y[0], y[1], y[2], y[3]), pk_fp8x4(y[4], y[5], y[6], y[7])};
;         const u32x4 wl = {cvtpk_h(y[0], y[1]), cvtpk_h(y[2], y[3]), cvtpk_h(y[4], y[5]), cvtpk_h(y[6], y[7])};
;         *(u32x4*)(H + 1024 + col) = wl; }
	v_add_f32_e32 v110, v114, v115
	v_lshlrev_b32_e32 v100, 16, v48
	v_and_b32_e32 v101, 0xffff0000, v48
	v_add_f32_e32 v106, v106, v110
	v_cvt_pk_f16_f32 v50, v102, v103
	v_pk_mul_f32 v[102:103], v[100:101], v[100:101]
	v_add_f32_e32 v106, v107, v106
	v_cvt_pk_f16_f32 v51, v52, v53
	v_cvt_pk_f16_f32 v52, v56, v57
	v_cvt_pk_f16_f32 v53, v54, v55
	v_lshlrev_b32_e32 v56, 16, v49
	v_and_b32_e32 v57, 0xffff0000, v49
	v_add_f32_e32 v102, v102, v106
	global_store_dwordx4 v[98:99], v[50:53], off offset:3328
	v_pk_mul_f32 v[98:99], v[56:57], v[56:57]
	v_add_f32_e32 v102, v103, v102
	v_lshlrev_b32_e32 v54, 16, v42
	v_and_b32_e32 v55, 0xffff0000, v42
	v_add_f32_e32 v98, v98, v102
	v_lshlrev_b32_e32 v46, 16, v45
	v_and_b32_e32 v47, 0xffff0000, v45
	v_lshlrev_b32_e32 v48, 16, v44
	v_and_b32_e32 v49, 0xffff0000, v44
	v_lshlrev_b32_e32 v44, 16, v43
	v_and_b32_e32 v45, 0xffff0000, v43
	v_pk_mul_f32 v[42:43], v[54:55], v[54:55]
	v_add_f32_e32 v98, v99, v98
	v_add_f32_e32 v42, v42, v98
	v_pk_mul_f32 v[120:121], v[44:45], v[44:45]
	v_add_f32_e32 v42, v43, v42
	v_add_f32_e32 v42, v120, v42
	v_pk_mul_f32 v[118:119], v[48:49], v[48:49]
	v_add_f32_e32 v42, v121, v42
	v_add_f32_e32 v42, v118, v42
	v_pk_mul_f32 v[116:117], v[46:47], v[46:47]
	v_add_f32_e32 v42, v119, v42
	v_add_f32_e32 v42, v116, v42
	v_add_f32_e32 v42, v117, v42
	v_mov_b32_e32 v43, v42
	s_nop 1
	v_permlane32_swap_b32 v42, v43
	s_nop 1
	v_lshl_add_u64 v[52:53], s[44:45], 0, v[82:83]
	v_add_f32_e32 v42, v42, v43
	ds_swizzle_b32 v43, v42 offset:swizzle(SWAP,16)
	v_add_co_u32_e32 v52, vcc, s35, v52
	v_lshl_add_u64 v[50:51], v[80:81], 0, v[178:179]
	s_nop 0
	v_addc_co_u32_e32 v53, vcc, 0, v53, vcc
	s_waitcnt lgkmcnt(0)
	v_add_f32_e32 v42, v42, v43
	v_add_co_u32_e32 v50, vcc, s35, v50
	s_nop 0
	v_add_f32_dpp v42, v42, v42 row_ror:8 row_mask:0xf bank_mask:0xf bound_ctrl:1
	v_addc_co_u32_e32 v51, vcc, 0, v51, vcc
	s_nop 0
	v_add_f32_dpp v42, v42, v42 row_ror:4 row_mask:0xf bank_mask:0xf bound_ctrl:1
	v_lshl_add_u64 v[80:81], v[80:81], 0, s[24:25]
	s_nop 0
	v_add_f32_dpp v42, v42, v42 quad_perm:[2,3,0,1] row_mask:0xf bank_mask:0xf bound_ctrl:1
	s_nop 1
	v_add_f32_dpp v42, v42, v42 quad_perm:[1,0,3,2] row_mask:0xf bank_mask:0xf bound_ctrl:1
	v_fmamk_f32 v42, v42, 0x3a800000, v0
	v_rsq_f32_e32 v42, v42
	s_nop 0
	v_pk_mul_f32 v[98:99], v[42:43], v[108:109] op_sel_hi:[0,1]
	v_pk_mul_f32 v[100:101], v[42:43], v[100:101] op_sel_hi:[0,1]
	v_pk_mul_f32 v[98:99], v[26:27], v[98:99]
	v_pk_mul_f32 v[100:101], v[30:31], v[100:101]
	v_pk_fma_f32 v[98:99], v[58:59], v[98:99], v[18:19]
	v_pk_fma_f32 v[100:101], v[60:61], v[100:101], v[22:23]
	v_pk_mul_f32 v[102:103], v[42:43], v[104:105] op_sel_hi:[0,1]
	v_mov_b32_e32 v104, 0
	v_mov_b32_e32 v105, 0
	v_pk_mul_f32 v[56:57], v[42:43], v[56:57] op_sel_hi:[0,1]
	v_cvt_pk_fp8_f32 v104, v98, v99
	v_cvt_pk_fp8_f32 v105, v100, v101
	v_pk_mul_f32 v[54:55], v[42:43], v[54:55] op_sel_hi:[0,1]
	v_pk_mul_f32 v[48:49], v[42:43], v[48:49] op_sel_hi:[0,1]
	v_pk_mul_f32 v[44:45], v[42:43], v[44:45] op_sel_hi:[0,1]
	v_pk_mul_f32 v[42:43], v[42:43], v[46:47] op_sel_hi:[0,1]
	v_pk_mul_f32 v[54:55], v[10:11], v[54:55]
	v_pk_mul_f32 v[48:49], v[14:15], v[48:49]
	v_pk_mul_f32 v[42:43], v[16:17], v[42:43]
	v_pk_mul_f32 v[102:103], v[28:29], v[102:103]
	v_pk_mul_f32 v[56:57], v[32:33], v[56:57]
	v_pk_fma_f32 v[54:55], v[66:67], v[54:55], v[2:3]
	v_pk_fma_f32 v[48:49], v[68:69], v[48:49], v[6:7]
	v_pk_fma_f32 v[46:47], v[72:73], v[42:43], v[8:9]
	v_mov_b32_e32 v42, 0
	v_mov_b32_e32 v43, 0
	v_pk_fma_f32 v[102:103], v[62:63], v[102:103], v[20:21]
	v_pk_fma_f32 v[56:57], v[64:65], v[56:57], v[24:25]
	v_cvt_pk_fp8_f32 v42, v54, v55
	v_cvt_pk_fp8_f32 v43, v48, v49
	v_cvt_pk_fp8_f32 v104, v102, v103 op_sel:[0,0,1]
	v_cvt_pk_fp8_f32 v105, v56, v57 op_sel:[0,0,1]
	v_pk_mul_f32 v[44:45], v[12:13], v[44:45]
	v_cvt_pk_f16_f32 v98, v98, v99
	v_pk_fma_f32 v[44:45], v[70:71], v[44:45], v[4:5]
	v_cvt_pk_f16_f32 v99, v102, v103
	v_cvt_pk_f16_f32 v100, v100, v101
	v_cvt_pk_f16_f32 v101, v56, v57
	v_cvt_pk_fp8_f32 v42, v44, v45 op_sel:[0,0,1]
	v_cvt_pk_fp8_f32 v43, v46, v47 op_sel:[0,0,1]
	global_store_dwordx2 v[52:53], v[104:105], off offset:256
	global_store_dwordx4 v[50:51], v[98:101], off offset:2304
	v_lshlrev_b32_e32 v56, 16, v39
	v_and_b32_e32 v57, 0xffff0000, v39
	v_lshlrev_b32_e32 v100, 16, v38
	v_and_b32_e32 v101, 0xffff0000, v38
	v_pk_mul_f32 v[102:103], v[100:101], v[100:101]
	v_pk_mul_f32 v[98:99], v[56:57], v[56:57]
	v_add_f32_e32 v102, v102, v103
	global_store_dwordx2 v[52:53], v[42:43], off offset:768
	v_lshlrev_b32_e32 v52, 16, v40
	v_and_b32_e32 v53, 0xffff0000, v40
	v_add_f32_e32 v98, v98, v102
	v_cvt_pk_f16_f32 v42, v54, v55
	v_pk_mul_f32 v[54:55], v[52:53], v[52:53]
	v_add_f32_e32 v98, v99, v98
	v_cvt_pk_f16_f32 v43, v44, v45
	v_cvt_pk_f16_f32 v44, v48, v49
	v_cvt_pk_f16_f32 v45, v46, v47
	v_lshlrev_b32_e32 v48, 16, v41
	v_and_b32_e32 v49, 0xffff0000, v41
	v_add_f32_e32 v54, v54, v98
	global_store_dwordx4 v[50:51], v[42:45], off offset:3328
	v_pk_mul_f32 v[50:51], v[48:49], v[48:49]
	v_add_f32_e32 v54, v55, v54
	v_lshlrev_b32_e32 v46, 16, v34
	v_and_b32_e32 v47, 0xffff0000, v34
	v_add_f32_e32 v50, v50, v54
	v_lshlrev_b32_e32 v38, 16, v37
	v_and_b32_e32 v39, 0xffff0000, v37
	v_lshlrev_b32_e32 v40, 16, v36
	v_and_b32_e32 v41, 0xffff0000, v36
	v_lshlrev_b32_e32 v36, 16, v35
	v_and_b32_e32 v37, 0xffff0000, v35
	v_pk_mul_f32 v[34:35], v[46:47], v[46:47]
	v_add_f32_e32 v50, v51, v50
	v_add_f32_e32 v34, v34, v50
	v_pk_mul_f32 v[108:109], v[36:37], v[36:37]
	v_add_f32_e32 v34, v35, v34
	v_add_f32_e32 v34, v108, v34
	v_pk_mul_f32 v[106:107], v[40:41], v[40:41]
	v_add_f32_e32 v34, v109, v34
	v_add_f32_e32 v34, v106, v34
	v_pk_mul_f32 v[104:105], v[38:39], v[38:39]
	v_add_f32_e32 v34, v107, v34
	v_add_f32_e32 v34, v104, v34
	v_add_f32_e32 v34, v105, v34
	v_mov_b32_e32 v35, v34
	s_nop 1
	v_permlane32_swap_b32 v34, v35
	s_nop 1
	v_lshl_add_u64 v[44:45], s[44:45], 0, v[76:77]
	v_add_f32_e32 v34, v34, v35
	ds_swizzle_b32 v35, v34 offset:swizzle(SWAP,16)
	v_add_co_u32_e32 v44, vcc, s35, v44
	v_lshl_add_u64 v[42:43], v[74:75], 0, v[178:179]
	s_nop 0
	v_addc_co_u32_e32 v45, vcc, 0, v45, vcc
	s_waitcnt lgkmcnt(0)
; DEV unsigned cvtpk_h(float lo, float hi) { f32x2 v = {lo, hi}; f16x2 r = __builtin_convertvector(v, f16x2); return __builtin_bit_cast(unsigned, r); }
; DEV unsigned pk_fp8x4(float a, float b, float c, float d) { int w = __builtin_amdgcn_cvt_pk_fp8_f32(a, b, 0, false); w = __builtin_amdgcn_cvt_pk_fp8_f32(c, d, w, true); return (unsigned)w; }
; DEV float fast_rsq(float x) { return __builtin_amdgcn_rsqf(x); }
; DEV float wave_sum(float v) { v = half_sum(v); v += lx16(v); v += lr8(v); v += lr4(v); v += lx2(v); v += lx1(v); return v; }
; DEV void norm_store_ffn(const Params& p, int tok, const float (&xv)[2][8], const NormRegs& nr, int lane) {
;     float ss = 0.f;
; #pragma unroll
;     for (int j = 0; j < 2; ++j)
; #pragma unroll
;         for (int i = 0; i < 8; ++i) ss += xv[j][i] * xv[j][i];
;     ss = wave_sum(ss);
;     const float rinv = fast_rsq(ss * (1.0f / 1024.0f) + EPS);
;     bf16_t* H = (bf16_t*)(p.ws + WS_H) + (size_t)tok * HLD;
; #pragma unroll
;     for (int j = 0; j < 2; ++j) { const int col = 8 * lane + 512 * j; float y[8];
; #pragma unroll
;         for (int i = 0; i < 4; ++i) { y[i] = xv[j][i] * rinv * nr.g[j][0][i] * (1.0f + nr.s[j][0][i]) + nr.h[j][0][i]; y[4 + i] = xv[j][4 + i] * rinv * nr.g[j][1][i] * (1.0f + nr.s[j][1][i]) + nr.h[j][1][i]; }
;         *(u32x2*)((unsigned char*)H + col) = (u32x2){pk_fp8x4(y[0], y[1], y[2], y[3]), pk_fp8x4(y[4], y[5], y[6], y[7])};
;         const u32x4 wl = {cvtpk_h(y[0], y[1]), cvtpk_h(y[2], y[3]), cvtpk_h(y[4], y[5]), cvtpk_h(y[6], y[7])};
;         *(u32x4*)(H + 1024 + col) = wl; }
	v_add_f32_e32 v34, v34, v35
	v_add_co_u32_e32 v42, vcc, s35, v42
	s_nop 0
	v_add_f32_dpp v34, v34, v34 row_ror:8 row_mask:0xf bank_mask:0xf bound_ctrl:1
	v_addc_co_u32_e32 v43, vcc, 0, v43, vcc
	s_nop 0
	v_add_f32_dpp v34, v34, v34 row_ror:4 row_mask:0xf bank_mask:0xf bound_ctrl:1
	s_add_u32 s44, s44, 0x21000
	s_addc_u32 s45, s45, 0
	v_add_f32_dpp v34, v34, v34 quad_perm:[2,3,0,1] row_mask:0xf bank_mask:0xf bound_ctrl:1
	v_cmp_lt_i32_e32 vcc, s2, v112
	v_lshl_add_u64 v[74:75], v[74:75], 0, s[24:25]
	v_add_f32_dpp v34, v34, v34 quad_perm:[1,0,3,2] row_mask:0xf bank_mask:0xf bound_ctrl:1
	v_fmamk_f32 v34, v34, 0x3a800000, v0
	v_rsq_f32_e32 v34, v34
	s_or_b64 s[42:43], vcc, s[42:43]
	v_pk_mul_f32 v[50:51], v[34:35], v[100:101] op_sel_hi:[0,1]
	v_pk_mul_f32 v[52:53], v[34:35], v[52:53] op_sel_hi:[0,1]
	v_pk_mul_f32 v[48:49], v[34:35], v[48:49] op_sel_hi:[0,1]
	v_pk_mul_f32 v[50:51], v[26:27], v[50:51]
	v_pk_mul_f32 v[52:53], v[30:31], v[52:53]
	v_pk_mul_f32 v[54:55], v[34:35], v[56:57] op_sel_hi:[0,1]
	v_pk_mul_f32 v[48:49], v[32:33], v[48:49]
	v_pk_mul_f32 v[46:47], v[34:35], v[46:47] op_sel_hi:[0,1]
	v_pk_mul_f32 v[40:41], v[34:35], v[40:41] op_sel_hi:[0,1]
	v_pk_mul_f32 v[36:37], v[34:35], v[36:37] op_sel_hi:[0,1]
	v_pk_mul_f32 v[34:35], v[34:35], v[38:39] op_sel_hi:[0,1]
	v_pk_fma_f32 v[50:51], v[58:59], v[50:51], v[18:19]
	v_pk_fma_f32 v[52:53], v[60:61], v[52:53], v[22:23]
	v_pk_fma_f32 v[56:57], v[64:65], v[48:49], v[24:25]
	v_mov_b32_e32 v48, 0
	v_mov_b32_e32 v49, 0
	v_pk_mul_f32 v[46:47], v[10:11], v[46:47]
	v_pk_mul_f32 v[40:41], v[14:15], v[40:41]
	v_pk_mul_f32 v[34:35], v[16:17], v[34:35]
	v_cvt_pk_fp8_f32 v48, v50, v51
	v_cvt_pk_fp8_f32 v49, v52, v53
	v_pk_fma_f32 v[46:47], v[66:67], v[46:47], v[2:3]
	v_pk_fma_f32 v[40:41], v[68:69], v[40:41], v[6:7]
	v_pk_fma_f32 v[38:39], v[72:73], v[34:35], v[8:9]
	v_mov_b32_e32 v34, 0
	v_mov_b32_e32 v35, 0
	v_cvt_pk_fp8_f32 v34, v46, v47
	v_cvt_pk_fp8_f32 v35, v40, v41
	v_pk_mul_f32 v[54:55], v[28:29], v[54:55]
	v_pk_mul_f32 v[36:37], v[12:13], v[36:37]
	v_pk_fma_f32 v[54:55], v[62:63], v[54:55], v[20:21]
	v_cvt_pk_fp8_f32 v49, v56, v57 op_sel:[0,0,1]
	v_cvt_pk_fp8_f32 v48, v54, v55 op_sel:[0,0,1]
	v_pk_fma_f32 v[36:37], v[70:71], v[36:37], v[4:5]
	v_cvt_pk_fp8_f32 v35, v38, v39 op_sel:[0,0,1]
	v_cvt_pk_fp8_f32 v34, v36, v37 op_sel:[0,0,1]
	global_store_dwordx2 v[44:45], v[48:49], off offset:256
	v_cvt_pk_f16_f32 v48, v50, v51
	v_cvt_pk_f16_f32 v49, v54, v55
	v_cvt_pk_f16_f32 v50, v52, v53
	v_cvt_pk_f16_f32 v51, v56, v57
	global_store_dwordx4 v[42:43], v[48:51], off offset:2304
	global_store_dwordx2 v[44:45], v[34:35], off offset:768
	v_cvt_pk_f16_f32 v34, v46, v47
	v_cvt_pk_f16_f32 v35, v36, v37
	v_cvt_pk_f16_f32 v36, v40, v41
	v_cvt_pk_f16_f32 v37, v38, v39
	global_store_dwordx4 v[42:43], v[34:37], off offset:3328
	s_waitcnt vmcnt(16)
	s_andn2_b64 exec, exec, s[42:43]
	s_cbranch_execnz .LBB0_1089
